# baseline (speedup 1.0000x reference)
_Z5k_aggPKDF16_PKhPKiS4_PKDv8_DF16_PKfPDF16_Pf:
	s_load_dwordx8 s[4:11], s[0:1], 0x8
	s_load_dwordx4 s[12:15], s[0:1], 0x28
	s_load_dwordx2 s[16:17], s[0:1], 0x38
	v_lshlrev_b32_e32 v2, 4, v0
	s_lshl_b32 s0, s2, 2
	s_lshl_b32 s1, s2, 3
	s_andn2_b32 s0, s0, 63
	s_and_b32 s1, s1, 56
	s_or_b32 s0, s0, s1
	s_lshr_b32 s1, s2, 1
	s_and_b32 s1, s1, 4
	s_or_b32 s0, s0, s1
	v_lshlrev_b32_e32 v1, 2, v0
	v_lshrrev_b32_e32 v52, 6, v0
	v_or_b32_e32 v3, s0, v52
	v_mov_b32_e32 v98, v2
	s_waitcnt lgkmcnt(0)
	global_load_dwordx4 v[64:67], v2, s[10:11]
	v_add_u32_e32 v96, 0x1000, v2
	global_load_dwordx4 v[68:71], v96, s[10:11]
	v_add_u32_e32 v96, 0x2000, v2
	global_load_dwordx4 v[72:75], v96, s[10:11]
	v_add_u32_e32 v96, 0x3000, v2
	global_load_dwordx4 v[76:79], v96, s[10:11]
	v_add_u32_e32 v96, 0x4000, v2
	global_load_dwordx4 v[80:83], v96, s[10:11]
	v_add_u32_e32 v96, 0x5000, v2
	global_load_dwordx4 v[84:87], v96, s[10:11]
	v_add_u32_e32 v96, 0x6000, v2
	global_load_dwordx4 v[88:91], v96, s[10:11]
	v_add_u32_e32 v96, 0x7000, v2
	global_load_dwordx4 v[92:95], v96, s[10:11]
	v_mov_b32_e32 v97, 0
	ds_write2st64_b32 v1, v97, v97 offset0:128 offset1:132
	ds_write2st64_b32 v1, v97, v97 offset0:136 offset1:140
	s_movk_i32 s0, 0x186a
	v_cmp_gt_i32_e32 vcc, s0, v3
	s_and_saveexec_b64 s[0:1], vcc
	s_cbranch_execz .Lagg_invalid
	v_bfe_u32 v4, v0, 2, 4
	v_lshlrev_b32_e32 v53, 4, v3
	v_or_b32_e32 v10, v53, v4
	v_and_b32_e32 v54, 48, v2
	v_lshl_or_b32 v11, v10, 7, v54
	global_load_dwordx4 v[2:5], v11, s[4:5]
	global_load_dwordx4 v[6:9], v11, s[4:5] offset:64
	v_ashrrev_i32_e32 v11, 31, v10
	v_lshl_add_u64 v[10:11], v[10:11], 2, s[6:7]
	global_load_dwordx2 v[50:51], v[10:11], off
	s_waitcnt vmcnt(3)
	ds_write_b128 v98, v[64:67]
	ds_write_b128 v98, v[68:71] offset:4096
	ds_write_b128 v98, v[72:75] offset:8192
	ds_write_b128 v98, v[76:79] offset:12288
	ds_write_b128 v98, v[80:83] offset:16384
	ds_write_b128 v98, v[84:87] offset:20480
	ds_write_b128 v98, v[88:91] offset:24576
	ds_write_b128 v98, v[92:95] offset:28672
	s_waitcnt vmcnt(2)
	v_cvt_pk_f32_fp8_e32 v[10:11], v2
	v_cvt_pk_f32_fp8_sdwa v[12:13], v2 src0_sel:WORD_1
	v_cvt_pk_f32_fp8_e32 v[14:15], v3
	v_cvt_pk_f32_fp8_sdwa v[2:3], v3 src0_sel:WORD_1
	v_cvt_pk_f32_fp8_e32 v[16:17], v4
	v_cvt_pk_f32_fp8_sdwa v[18:19], v4 src0_sel:WORD_1
	v_cvt_pk_f32_fp8_e32 v[20:21], v5
	v_cvt_pk_f32_fp8_sdwa v[4:5], v5 src0_sel:WORD_1
	s_waitcnt vmcnt(1)
	v_cvt_pk_f32_fp8_e32 v[22:23], v6
	v_cvt_pk_f32_fp8_sdwa v[24:25], v6 src0_sel:WORD_1
	v_cvt_pk_f32_fp8_e32 v[26:27], v7
	v_cvt_pk_f32_fp8_sdwa v[6:7], v7 src0_sel:WORD_1
	v_cvt_pk_f32_fp8_e32 v[28:29], v8
	v_cvt_pk_f32_fp8_sdwa v[30:31], v8 src0_sel:WORD_1
	v_cvt_pk_f32_fp8_e32 v[32:33], v9
	v_cvt_pk_f32_fp8_sdwa v[8:9], v9 src0_sel:WORD_1
	v_add_f32_e32 v88, 0, v10
	v_add_f32_e32 v89, 0, v11
	v_add_f32_e32 v90, 0, v12
	v_add_f32_e32 v91, 0, v13
	v_add_f32_e32 v92, 0, v14
	v_add_f32_e32 v93, 0, v15
	v_add_f32_e32 v94, 0, v2
	v_add_f32_e32 v95, 0, v3
	v_add_f32_e32 v76, 0, v16
	v_add_f32_e32 v77, 0, v17
	v_add_f32_e32 v80, 0, v18
	v_add_f32_e32 v81, 0, v19
	v_add_f32_e32 v84, 0, v20
	v_add_f32_e32 v85, 0, v21
	v_add_f32_e32 v86, 0, v4
	v_add_f32_e32 v87, 0, v5
	v_add_f32_e32 v72, 0, v22
	v_add_f32_e32 v73, 0, v23
	v_add_f32_e32 v74, 0, v24
	v_add_f32_e32 v75, 0, v25
	v_add_f32_e32 v78, 0, v26
	v_add_f32_e32 v79, 0, v27
	v_add_f32_e32 v82, 0, v6
	v_add_f32_e32 v83, 0, v7
	v_add_f32_e32 v64, 0, v28
	v_add_f32_e32 v65, 0, v29
	v_add_f32_e32 v66, 0, v30
	v_add_f32_e32 v67, 0, v31
	v_add_f32_e32 v68, 0, v32
	v_add_f32_e32 v69, 0, v33
	v_add_f32_e32 v70, 0, v8
	v_add_f32_e32 v71, 0, v9
	s_waitcnt vmcnt(0)
	s_mov_b64 s[6:7], exec
	v_mov_b32_e32 v63, 0xc35000
	v_add_u32_e32 v106, 0, v50
	v_lshlrev_b32_e32 v106, 2, v106
	global_load_dwordx3 v[56:58], v106, s[8:9]
	v_add_u32_e32 v106, 3, v50
	v_lshlrev_b32_e32 v106, 2, v106
	global_load_dwordx3 v[60:62], v106, s[8:9]
	s_waitcnt vmcnt(0)
	v_add_u32_e32 v104, 0, v50
	v_cmp_lt_i32_e32 vcc, v104, v51
	v_lshlrev_b32_e32 v105, 7, v56
	s_nop 0
	v_cndmask_b32_e32 v105, v63, v105, vcc
	v_or_b32_e32 v105, v54, v105
	global_load_dwordx4 v[2:5], v105, s[4:5]
	global_load_dwordx4 v[6:9], v105, s[4:5] offset:64
	v_add_u32_e32 v104, 1, v50
	v_cmp_lt_i32_e32 vcc, v104, v51
	v_lshlrev_b32_e32 v105, 7, v57
	s_nop 0
	v_cndmask_b32_e32 v105, v63, v105, vcc
	v_or_b32_e32 v105, v54, v105
	global_load_dwordx4 v[10:13], v105, s[4:5]
	global_load_dwordx4 v[14:17], v105, s[4:5] offset:64
	v_add_u32_e32 v104, 2, v50
	v_cmp_lt_i32_e32 vcc, v104, v51
	v_lshlrev_b32_e32 v105, 7, v58
	s_nop 0
	v_cndmask_b32_e32 v105, v63, v105, vcc
	v_or_b32_e32 v105, v54, v105
	global_load_dwordx4 v[18:21], v105, s[4:5]
	global_load_dwordx4 v[22:25], v105, s[4:5] offset:64
	v_add_u32_e32 v106, 6, v50
	v_lshlrev_b32_e32 v106, 2, v106
	global_load_dwordx3 v[56:58], v106, s[8:9]
	v_add_u32_e32 v104, 3, v50
	v_cmp_lt_i32_e32 vcc, v104, v51
	v_lshlrev_b32_e32 v105, 7, v60
	s_nop 0
	v_cndmask_b32_e32 v105, v63, v105, vcc
	v_or_b32_e32 v105, v54, v105
	global_load_dwordx4 v[26:29], v105, s[4:5]
	global_load_dwordx4 v[30:33], v105, s[4:5] offset:64
	v_add_u32_e32 v104, 4, v50
	v_cmp_lt_i32_e32 vcc, v104, v51
	v_lshlrev_b32_e32 v105, 7, v61
	s_nop 0
	v_cndmask_b32_e32 v105, v63, v105, vcc
	v_or_b32_e32 v105, v54, v105
	global_load_dwordx4 v[34:37], v105, s[4:5]
	global_load_dwordx4 v[38:41], v105, s[4:5] offset:64
	v_add_u32_e32 v104, 5, v50
	v_cmp_lt_i32_e32 vcc, v104, v51
	v_lshlrev_b32_e32 v105, 7, v62
	s_nop 0
	v_cndmask_b32_e32 v105, v63, v105, vcc
	v_or_b32_e32 v105, v54, v105
	global_load_dwordx4 v[42:45], v105, s[4:5]
	global_load_dwordx4 v[46:49], v105, s[4:5] offset:64
	v_add_u32_e32 v106, 9, v50
	v_lshlrev_b32_e32 v106, 2, v106
	global_load_dwordx3 v[60:62], v106, s[8:9]
.Lagg_gloop:
	v_add_u32_e32 v104, 6, v50
	v_cmp_lt_i32_e32 vcc, v104, v51
	s_and_b64 vcc, exec, vcc
	s_cbranch_scc0 .Lagg_glast
	s_waitcnt vmcnt(7)
	v_cvt_pk_f32_fp8_e32 v[96:97], v2
	v_cvt_pk_f32_fp8_sdwa v[98:99], v2 src0_sel:WORD_1
	v_cvt_pk_f32_fp8_e32 v[100:101], v3
	v_cvt_pk_f32_fp8_sdwa v[102:103], v3 src0_sel:WORD_1
	v_pk_add_f32 v[88:89], v[88:89], v[96:97]
	v_pk_add_f32 v[90:91], v[90:91], v[98:99]
	v_pk_add_f32 v[92:93], v[92:93], v[100:101]
	v_pk_add_f32 v[94:95], v[94:95], v[102:103]
	v_cvt_pk_f32_fp8_e32 v[96:97], v4
	v_cvt_pk_f32_fp8_sdwa v[98:99], v4 src0_sel:WORD_1
	v_cvt_pk_f32_fp8_e32 v[100:101], v5
	v_cvt_pk_f32_fp8_sdwa v[102:103], v5 src0_sel:WORD_1
	v_pk_add_f32 v[76:77], v[76:77], v[96:97]
	v_pk_add_f32 v[80:81], v[80:81], v[98:99]
	v_pk_add_f32 v[84:85], v[84:85], v[100:101]
	v_pk_add_f32 v[86:87], v[86:87], v[102:103]
	v_cvt_pk_f32_fp8_e32 v[96:97], v6
	v_cvt_pk_f32_fp8_sdwa v[98:99], v6 src0_sel:WORD_1
	v_cvt_pk_f32_fp8_e32 v[100:101], v7
	v_cvt_pk_f32_fp8_sdwa v[102:103], v7 src0_sel:WORD_1
	v_pk_add_f32 v[72:73], v[72:73], v[96:97]
	v_pk_add_f32 v[74:75], v[74:75], v[98:99]
	v_pk_add_f32 v[78:79], v[78:79], v[100:101]
	v_pk_add_f32 v[82:83], v[82:83], v[102:103]
	v_cvt_pk_f32_fp8_e32 v[96:97], v8
	v_cvt_pk_f32_fp8_sdwa v[98:99], v8 src0_sel:WORD_1
	v_cvt_pk_f32_fp8_e32 v[100:101], v9
	v_cvt_pk_f32_fp8_sdwa v[102:103], v9 src0_sel:WORD_1
	v_pk_add_f32 v[64:65], v[64:65], v[96:97]
	v_pk_add_f32 v[66:67], v[66:67], v[98:99]
	v_pk_add_f32 v[68:69], v[68:69], v[100:101]
	v_pk_add_f32 v[70:71], v[70:71], v[102:103]
	v_add_u32_e32 v104, 6, v50
	v_cmp_lt_i32_e32 vcc, v104, v51
	v_lshlrev_b32_e32 v105, 7, v56
	s_nop 0
	v_cndmask_b32_e32 v105, v63, v105, vcc
	v_or_b32_e32 v105, v54, v105
	global_load_dwordx4 v[2:5], v105, s[4:5]
	global_load_dwordx4 v[6:9], v105, s[4:5] offset:64
	s_waitcnt vmcnt(9)
	v_cvt_pk_f32_fp8_e32 v[96:97], v10
	v_cvt_pk_f32_fp8_sdwa v[98:99], v10 src0_sel:WORD_1
	v_cvt_pk_f32_fp8_e32 v[100:101], v11
	v_cvt_pk_f32_fp8_sdwa v[102:103], v11 src0_sel:WORD_1
	v_pk_add_f32 v[88:89], v[88:89], v[96:97]
	v_pk_add_f32 v[90:91], v[90:91], v[98:99]
	v_pk_add_f32 v[92:93], v[92:93], v[100:101]
	v_pk_add_f32 v[94:95], v[94:95], v[102:103]
	v_cvt_pk_f32_fp8_e32 v[96:97], v12
	v_cvt_pk_f32_fp8_sdwa v[98:99], v12 src0_sel:WORD_1
	v_cvt_pk_f32_fp8_e32 v[100:101], v13
	v_cvt_pk_f32_fp8_sdwa v[102:103], v13 src0_sel:WORD_1
	v_pk_add_f32 v[76:77], v[76:77], v[96:97]
	v_pk_add_f32 v[80:81], v[80:81], v[98:99]
	v_pk_add_f32 v[84:85], v[84:85], v[100:101]
	v_pk_add_f32 v[86:87], v[86:87], v[102:103]
	v_cvt_pk_f32_fp8_e32 v[96:97], v14
	v_cvt_pk_f32_fp8_sdwa v[98:99], v14 src0_sel:WORD_1
	v_cvt_pk_f32_fp8_e32 v[100:101], v15
	v_cvt_pk_f32_fp8_sdwa v[102:103], v15 src0_sel:WORD_1
	v_pk_add_f32 v[72:73], v[72:73], v[96:97]
	v_pk_add_f32 v[74:75], v[74:75], v[98:99]
	v_pk_add_f32 v[78:79], v[78:79], v[100:101]
	v_pk_add_f32 v[82:83], v[82:83], v[102:103]
	v_cvt_pk_f32_fp8_e32 v[96:97], v16
	v_cvt_pk_f32_fp8_sdwa v[98:99], v16 src0_sel:WORD_1
	v_cvt_pk_f32_fp8_e32 v[100:101], v17
	v_cvt_pk_f32_fp8_sdwa v[102:103], v17 src0_sel:WORD_1
	v_pk_add_f32 v[64:65], v[64:65], v[96:97]
	v_pk_add_f32 v[66:67], v[66:67], v[98:99]
	v_pk_add_f32 v[68:69], v[68:69], v[100:101]
	v_pk_add_f32 v[70:71], v[70:71], v[102:103]
	v_add_u32_e32 v104, 7, v50
	v_cmp_lt_i32_e32 vcc, v104, v51
	v_lshlrev_b32_e32 v105, 7, v57
	s_nop 0
	v_cndmask_b32_e32 v105, v63, v105, vcc
	v_or_b32_e32 v105, v54, v105
	global_load_dwordx4 v[10:13], v105, s[4:5]
	global_load_dwordx4 v[14:17], v105, s[4:5] offset:64
	s_waitcnt vmcnt(11)
	v_cvt_pk_f32_fp8_e32 v[96:97], v18
	v_cvt_pk_f32_fp8_sdwa v[98:99], v18 src0_sel:WORD_1
	v_cvt_pk_f32_fp8_e32 v[100:101], v19
	v_cvt_pk_f32_fp8_sdwa v[102:103], v19 src0_sel:WORD_1
	v_pk_add_f32 v[88:89], v[88:89], v[96:97]
	v_pk_add_f32 v[90:91], v[90:91], v[98:99]
	v_pk_add_f32 v[92:93], v[92:93], v[100:101]
	v_pk_add_f32 v[94:95], v[94:95], v[102:103]
	v_cvt_pk_f32_fp8_e32 v[96:97], v20
	v_cvt_pk_f32_fp8_sdwa v[98:99], v20 src0_sel:WORD_1
	v_cvt_pk_f32_fp8_e32 v[100:101], v21
	v_cvt_pk_f32_fp8_sdwa v[102:103], v21 src0_sel:WORD_1
	v_pk_add_f32 v[76:77], v[76:77], v[96:97]
	v_pk_add_f32 v[80:81], v[80:81], v[98:99]
	v_pk_add_f32 v[84:85], v[84:85], v[100:101]
	v_pk_add_f32 v[86:87], v[86:87], v[102:103]
	v_cvt_pk_f32_fp8_e32 v[96:97], v22
	v_cvt_pk_f32_fp8_sdwa v[98:99], v22 src0_sel:WORD_1
	v_cvt_pk_f32_fp8_e32 v[100:101], v23
	v_cvt_pk_f32_fp8_sdwa v[102:103], v23 src0_sel:WORD_1
	v_pk_add_f32 v[72:73], v[72:73], v[96:97]
	v_pk_add_f32 v[74:75], v[74:75], v[98:99]
	v_pk_add_f32 v[78:79], v[78:79], v[100:101]
	v_pk_add_f32 v[82:83], v[82:83], v[102:103]
	v_cvt_pk_f32_fp8_e32 v[96:97], v24
	v_cvt_pk_f32_fp8_sdwa v[98:99], v24 src0_sel:WORD_1
	v_cvt_pk_f32_fp8_e32 v[100:101], v25
	v_cvt_pk_f32_fp8_sdwa v[102:103], v25 src0_sel:WORD_1
	v_pk_add_f32 v[64:65], v[64:65], v[96:97]
	v_pk_add_f32 v[66:67], v[66:67], v[98:99]
	v_pk_add_f32 v[68:69], v[68:69], v[100:101]
	v_pk_add_f32 v[70:71], v[70:71], v[102:103]
	v_add_u32_e32 v104, 8, v50
	v_cmp_lt_i32_e32 vcc, v104, v51
	v_lshlrev_b32_e32 v105, 7, v58
	s_nop 0
	v_cndmask_b32_e32 v105, v63, v105, vcc
	v_or_b32_e32 v105, v54, v105
	global_load_dwordx4 v[18:21], v105, s[4:5]
	global_load_dwordx4 v[22:25], v105, s[4:5] offset:64
	v_add_u32_e32 v106, 12, v50
	v_lshlrev_b32_e32 v106, 2, v106
	global_load_dwordx3 v[56:58], v106, s[8:9]
	s_waitcnt vmcnt(7)
	v_cvt_pk_f32_fp8_e32 v[96:97], v26
	v_cvt_pk_f32_fp8_sdwa v[98:99], v26 src0_sel:WORD_1
	v_cvt_pk_f32_fp8_e32 v[100:101], v27
	v_cvt_pk_f32_fp8_sdwa v[102:103], v27 src0_sel:WORD_1
	v_pk_add_f32 v[88:89], v[88:89], v[96:97]
	v_pk_add_f32 v[90:91], v[90:91], v[98:99]
	v_pk_add_f32 v[92:93], v[92:93], v[100:101]
	v_pk_add_f32 v[94:95], v[94:95], v[102:103]
	v_cvt_pk_f32_fp8_e32 v[96:97], v28
	v_cvt_pk_f32_fp8_sdwa v[98:99], v28 src0_sel:WORD_1
	v_cvt_pk_f32_fp8_e32 v[100:101], v29
	v_cvt_pk_f32_fp8_sdwa v[102:103], v29 src0_sel:WORD_1
	v_pk_add_f32 v[76:77], v[76:77], v[96:97]
	v_pk_add_f32 v[80:81], v[80:81], v[98:99]
	v_pk_add_f32 v[84:85], v[84:85], v[100:101]
	v_pk_add_f32 v[86:87], v[86:87], v[102:103]
	v_cvt_pk_f32_fp8_e32 v[96:97], v30
	v_cvt_pk_f32_fp8_sdwa v[98:99], v30 src0_sel:WORD_1
	v_cvt_pk_f32_fp8_e32 v[100:101], v31
	v_cvt_pk_f32_fp8_sdwa v[102:103], v31 src0_sel:WORD_1
	v_pk_add_f32 v[72:73], v[72:73], v[96:97]
	v_pk_add_f32 v[74:75], v[74:75], v[98:99]
	v_pk_add_f32 v[78:79], v[78:79], v[100:101]
	v_pk_add_f32 v[82:83], v[82:83], v[102:103]
	v_cvt_pk_f32_fp8_e32 v[96:97], v32
	v_cvt_pk_f32_fp8_sdwa v[98:99], v32 src0_sel:WORD_1
	v_cvt_pk_f32_fp8_e32 v[100:101], v33
	v_cvt_pk_f32_fp8_sdwa v[102:103], v33 src0_sel:WORD_1
	v_pk_add_f32 v[64:65], v[64:65], v[96:97]
	v_pk_add_f32 v[66:67], v[66:67], v[98:99]
	v_pk_add_f32 v[68:69], v[68:69], v[100:101]
	v_pk_add_f32 v[70:71], v[70:71], v[102:103]
	v_add_u32_e32 v104, 9, v50
	v_cmp_lt_i32_e32 vcc, v104, v51
	v_lshlrev_b32_e32 v105, 7, v60
	s_nop 0
	v_cndmask_b32_e32 v105, v63, v105, vcc
	v_or_b32_e32 v105, v54, v105
	global_load_dwordx4 v[26:29], v105, s[4:5]
	global_load_dwordx4 v[30:33], v105, s[4:5] offset:64
	s_waitcnt vmcnt(9)
	v_cvt_pk_f32_fp8_e32 v[96:97], v34
	v_cvt_pk_f32_fp8_sdwa v[98:99], v34 src0_sel:WORD_1
	v_cvt_pk_f32_fp8_e32 v[100:101], v35
	v_cvt_pk_f32_fp8_sdwa v[102:103], v35 src0_sel:WORD_1
	v_pk_add_f32 v[88:89], v[88:89], v[96:97]
	v_pk_add_f32 v[90:91], v[90:91], v[98:99]
	v_pk_add_f32 v[92:93], v[92:93], v[100:101]
	v_pk_add_f32 v[94:95], v[94:95], v[102:103]
	v_cvt_pk_f32_fp8_e32 v[96:97], v36
	v_cvt_pk_f32_fp8_sdwa v[98:99], v36 src0_sel:WORD_1
	v_cvt_pk_f32_fp8_e32 v[100:101], v37
	v_cvt_pk_f32_fp8_sdwa v[102:103], v37 src0_sel:WORD_1
	v_pk_add_f32 v[76:77], v[76:77], v[96:97]
	v_pk_add_f32 v[80:81], v[80:81], v[98:99]
	v_pk_add_f32 v[84:85], v[84:85], v[100:101]
	v_pk_add_f32 v[86:87], v[86:87], v[102:103]
	v_cvt_pk_f32_fp8_e32 v[96:97], v38
	v_cvt_pk_f32_fp8_sdwa v[98:99], v38 src0_sel:WORD_1
	v_cvt_pk_f32_fp8_e32 v[100:101], v39
	v_cvt_pk_f32_fp8_sdwa v[102:103], v39 src0_sel:WORD_1
	v_pk_add_f32 v[72:73], v[72:73], v[96:97]
	v_pk_add_f32 v[74:75], v[74:75], v[98:99]
	v_pk_add_f32 v[78:79], v[78:79], v[100:101]
	v_pk_add_f32 v[82:83], v[82:83], v[102:103]
	v_cvt_pk_f32_fp8_e32 v[96:97], v40
	v_cvt_pk_f32_fp8_sdwa v[98:99], v40 src0_sel:WORD_1
	v_cvt_pk_f32_fp8_e32 v[100:101], v41
	v_cvt_pk_f32_fp8_sdwa v[102:103], v41 src0_sel:WORD_1
	v_pk_add_f32 v[64:65], v[64:65], v[96:97]
	v_pk_add_f32 v[66:67], v[66:67], v[98:99]
	v_pk_add_f32 v[68:69], v[68:69], v[100:101]
	v_pk_add_f32 v[70:71], v[70:71], v[102:103]
	v_add_u32_e32 v104, 10, v50
	v_cmp_lt_i32_e32 vcc, v104, v51
	v_lshlrev_b32_e32 v105, 7, v61
	s_nop 0
	v_cndmask_b32_e32 v105, v63, v105, vcc
	v_or_b32_e32 v105, v54, v105
	global_load_dwordx4 v[34:37], v105, s[4:5]
	global_load_dwordx4 v[38:41], v105, s[4:5] offset:64
	s_waitcnt vmcnt(11)
	v_cvt_pk_f32_fp8_e32 v[96:97], v42
	v_cvt_pk_f32_fp8_sdwa v[98:99], v42 src0_sel:WORD_1
	v_cvt_pk_f32_fp8_e32 v[100:101], v43
	v_cvt_pk_f32_fp8_sdwa v[102:103], v43 src0_sel:WORD_1
	v_pk_add_f32 v[88:89], v[88:89], v[96:97]
	v_pk_add_f32 v[90:91], v[90:91], v[98:99]
	v_pk_add_f32 v[92:93], v[92:93], v[100:101]
	v_pk_add_f32 v[94:95], v[94:95], v[102:103]
	v_cvt_pk_f32_fp8_e32 v[96:97], v44
	v_cvt_pk_f32_fp8_sdwa v[98:99], v44 src0_sel:WORD_1
	v_cvt_pk_f32_fp8_e32 v[100:101], v45
	v_cvt_pk_f32_fp8_sdwa v[102:103], v45 src0_sel:WORD_1
	v_pk_add_f32 v[76:77], v[76:77], v[96:97]
	v_pk_add_f32 v[80:81], v[80:81], v[98:99]
	v_pk_add_f32 v[84:85], v[84:85], v[100:101]
	v_pk_add_f32 v[86:87], v[86:87], v[102:103]
	v_cvt_pk_f32_fp8_e32 v[96:97], v46
	v_cvt_pk_f32_fp8_sdwa v[98:99], v46 src0_sel:WORD_1
	v_cvt_pk_f32_fp8_e32 v[100:101], v47
	v_cvt_pk_f32_fp8_sdwa v[102:103], v47 src0_sel:WORD_1
	v_pk_add_f32 v[72:73], v[72:73], v[96:97]
	v_pk_add_f32 v[74:75], v[74:75], v[98:99]
	v_pk_add_f32 v[78:79], v[78:79], v[100:101]
	v_pk_add_f32 v[82:83], v[82:83], v[102:103]
	v_cvt_pk_f32_fp8_e32 v[96:97], v48
	v_cvt_pk_f32_fp8_sdwa v[98:99], v48 src0_sel:WORD_1
	v_cvt_pk_f32_fp8_e32 v[100:101], v49
	v_cvt_pk_f32_fp8_sdwa v[102:103], v49 src0_sel:WORD_1
	v_pk_add_f32 v[64:65], v[64:65], v[96:97]
	v_pk_add_f32 v[66:67], v[66:67], v[98:99]
	v_pk_add_f32 v[68:69], v[68:69], v[100:101]
	v_pk_add_f32 v[70:71], v[70:71], v[102:103]
	v_add_u32_e32 v104, 11, v50
	v_cmp_lt_i32_e32 vcc, v104, v51
	v_lshlrev_b32_e32 v105, 7, v62
	s_nop 0
	v_cndmask_b32_e32 v105, v63, v105, vcc
	v_or_b32_e32 v105, v54, v105
	global_load_dwordx4 v[42:45], v105, s[4:5]
	global_load_dwordx4 v[46:49], v105, s[4:5] offset:64
	v_add_u32_e32 v106, 15, v50
	v_lshlrev_b32_e32 v106, 2, v106
	global_load_dwordx3 v[60:62], v106, s[8:9]
	v_add_u32_e32 v50, 6, v50
	s_branch .Lagg_gloop
.Lagg_glast:
	s_waitcnt vmcnt(12)
	v_cvt_pk_f32_fp8_e32 v[96:97], v2
	v_cvt_pk_f32_fp8_sdwa v[98:99], v2 src0_sel:WORD_1
	v_cvt_pk_f32_fp8_e32 v[100:101], v3
	v_cvt_pk_f32_fp8_sdwa v[102:103], v3 src0_sel:WORD_1
	v_pk_add_f32 v[88:89], v[88:89], v[96:97]
	v_pk_add_f32 v[90:91], v[90:91], v[98:99]
	v_pk_add_f32 v[92:93], v[92:93], v[100:101]
	v_pk_add_f32 v[94:95], v[94:95], v[102:103]
	v_cvt_pk_f32_fp8_e32 v[96:97], v4
	v_cvt_pk_f32_fp8_sdwa v[98:99], v4 src0_sel:WORD_1
	v_cvt_pk_f32_fp8_e32 v[100:101], v5
	v_cvt_pk_f32_fp8_sdwa v[102:103], v5 src0_sel:WORD_1
	v_pk_add_f32 v[76:77], v[76:77], v[96:97]
	v_pk_add_f32 v[80:81], v[80:81], v[98:99]
	v_pk_add_f32 v[84:85], v[84:85], v[100:101]
	v_pk_add_f32 v[86:87], v[86:87], v[102:103]
	v_cvt_pk_f32_fp8_e32 v[96:97], v6
	v_cvt_pk_f32_fp8_sdwa v[98:99], v6 src0_sel:WORD_1
	v_cvt_pk_f32_fp8_e32 v[100:101], v7
	v_cvt_pk_f32_fp8_sdwa v[102:103], v7 src0_sel:WORD_1
	v_pk_add_f32 v[72:73], v[72:73], v[96:97]
	v_pk_add_f32 v[74:75], v[74:75], v[98:99]
	v_pk_add_f32 v[78:79], v[78:79], v[100:101]
	v_pk_add_f32 v[82:83], v[82:83], v[102:103]
	v_cvt_pk_f32_fp8_e32 v[96:97], v8
	v_cvt_pk_f32_fp8_sdwa v[98:99], v8 src0_sel:WORD_1
	v_cvt_pk_f32_fp8_e32 v[100:101], v9
	v_cvt_pk_f32_fp8_sdwa v[102:103], v9 src0_sel:WORD_1
	v_pk_add_f32 v[64:65], v[64:65], v[96:97]
	v_pk_add_f32 v[66:67], v[66:67], v[98:99]
	v_pk_add_f32 v[68:69], v[68:69], v[100:101]
	v_pk_add_f32 v[70:71], v[70:71], v[102:103]
	s_waitcnt vmcnt(10)
	v_cvt_pk_f32_fp8_e32 v[96:97], v10
	v_cvt_pk_f32_fp8_sdwa v[98:99], v10 src0_sel:WORD_1
	v_cvt_pk_f32_fp8_e32 v[100:101], v11
	v_cvt_pk_f32_fp8_sdwa v[102:103], v11 src0_sel:WORD_1
	v_pk_add_f32 v[88:89], v[88:89], v[96:97]
	v_pk_add_f32 v[90:91], v[90:91], v[98:99]
	v_pk_add_f32 v[92:93], v[92:93], v[100:101]
	v_pk_add_f32 v[94:95], v[94:95], v[102:103]
	v_cvt_pk_f32_fp8_e32 v[96:97], v12
	v_cvt_pk_f32_fp8_sdwa v[98:99], v12 src0_sel:WORD_1
	v_cvt_pk_f32_fp8_e32 v[100:101], v13
	v_cvt_pk_f32_fp8_sdwa v[102:103], v13 src0_sel:WORD_1
	v_pk_add_f32 v[76:77], v[76:77], v[96:97]
	v_pk_add_f32 v[80:81], v[80:81], v[98:99]
	v_pk_add_f32 v[84:85], v[84:85], v[100:101]
	v_pk_add_f32 v[86:87], v[86:87], v[102:103]
	v_cvt_pk_f32_fp8_e32 v[96:97], v14
	v_cvt_pk_f32_fp8_sdwa v[98:99], v14 src0_sel:WORD_1
	v_cvt_pk_f32_fp8_e32 v[100:101], v15
	v_cvt_pk_f32_fp8_sdwa v[102:103], v15 src0_sel:WORD_1
	v_pk_add_f32 v[72:73], v[72:73], v[96:97]
	v_pk_add_f32 v[74:75], v[74:75], v[98:99]
	v_pk_add_f32 v[78:79], v[78:79], v[100:101]
	v_pk_add_f32 v[82:83], v[82:83], v[102:103]
	v_cvt_pk_f32_fp8_e32 v[96:97], v16
	v_cvt_pk_f32_fp8_sdwa v[98:99], v16 src0_sel:WORD_1
	v_cvt_pk_f32_fp8_e32 v[100:101], v17
	v_cvt_pk_f32_fp8_sdwa v[102:103], v17 src0_sel:WORD_1
	v_pk_add_f32 v[64:65], v[64:65], v[96:97]
	v_pk_add_f32 v[66:67], v[66:67], v[98:99]
	v_pk_add_f32 v[68:69], v[68:69], v[100:101]
	v_pk_add_f32 v[70:71], v[70:71], v[102:103]
	s_waitcnt vmcnt(8)
	v_cvt_pk_f32_fp8_e32 v[96:97], v18
	v_cvt_pk_f32_fp8_sdwa v[98:99], v18 src0_sel:WORD_1
	v_cvt_pk_f32_fp8_e32 v[100:101], v19
	v_cvt_pk_f32_fp8_sdwa v[102:103], v19 src0_sel:WORD_1
	v_pk_add_f32 v[88:89], v[88:89], v[96:97]
	v_pk_add_f32 v[90:91], v[90:91], v[98:99]
	v_pk_add_f32 v[92:93], v[92:93], v[100:101]
	v_pk_add_f32 v[94:95], v[94:95], v[102:103]
	v_cvt_pk_f32_fp8_e32 v[96:97], v20
	v_cvt_pk_f32_fp8_sdwa v[98:99], v20 src0_sel:WORD_1
	v_cvt_pk_f32_fp8_e32 v[100:101], v21
	v_cvt_pk_f32_fp8_sdwa v[102:103], v21 src0_sel:WORD_1
	v_pk_add_f32 v[76:77], v[76:77], v[96:97]
	v_pk_add_f32 v[80:81], v[80:81], v[98:99]
	v_pk_add_f32 v[84:85], v[84:85], v[100:101]
	v_pk_add_f32 v[86:87], v[86:87], v[102:103]
	v_cvt_pk_f32_fp8_e32 v[96:97], v22
	v_cvt_pk_f32_fp8_sdwa v[98:99], v22 src0_sel:WORD_1
	v_cvt_pk_f32_fp8_e32 v[100:101], v23
	v_cvt_pk_f32_fp8_sdwa v[102:103], v23 src0_sel:WORD_1
	v_pk_add_f32 v[72:73], v[72:73], v[96:97]
	v_pk_add_f32 v[74:75], v[74:75], v[98:99]
	v_pk_add_f32 v[78:79], v[78:79], v[100:101]
	v_pk_add_f32 v[82:83], v[82:83], v[102:103]
	v_cvt_pk_f32_fp8_e32 v[96:97], v24
	v_cvt_pk_f32_fp8_sdwa v[98:99], v24 src0_sel:WORD_1
	v_cvt_pk_f32_fp8_e32 v[100:101], v25
	v_cvt_pk_f32_fp8_sdwa v[102:103], v25 src0_sel:WORD_1
	v_pk_add_f32 v[64:65], v[64:65], v[96:97]
	v_pk_add_f32 v[66:67], v[66:67], v[98:99]
	v_pk_add_f32 v[68:69], v[68:69], v[100:101]
	v_pk_add_f32 v[70:71], v[70:71], v[102:103]
	s_waitcnt vmcnt(5)
	v_cvt_pk_f32_fp8_e32 v[96:97], v26
	v_cvt_pk_f32_fp8_sdwa v[98:99], v26 src0_sel:WORD_1
	v_cvt_pk_f32_fp8_e32 v[100:101], v27
	v_cvt_pk_f32_fp8_sdwa v[102:103], v27 src0_sel:WORD_1
	v_pk_add_f32 v[88:89], v[88:89], v[96:97]
	v_pk_add_f32 v[90:91], v[90:91], v[98:99]
	v_pk_add_f32 v[92:93], v[92:93], v[100:101]
	v_pk_add_f32 v[94:95], v[94:95], v[102:103]
	v_cvt_pk_f32_fp8_e32 v[96:97], v28
	v_cvt_pk_f32_fp8_sdwa v[98:99], v28 src0_sel:WORD_1
	v_cvt_pk_f32_fp8_e32 v[100:101], v29
	v_cvt_pk_f32_fp8_sdwa v[102:103], v29 src0_sel:WORD_1
	v_pk_add_f32 v[76:77], v[76:77], v[96:97]
	v_pk_add_f32 v[80:81], v[80:81], v[98:99]
	v_pk_add_f32 v[84:85], v[84:85], v[100:101]
	v_pk_add_f32 v[86:87], v[86:87], v[102:103]
	v_cvt_pk_f32_fp8_e32 v[96:97], v30
	v_cvt_pk_f32_fp8_sdwa v[98:99], v30 src0_sel:WORD_1
	v_cvt_pk_f32_fp8_e32 v[100:101], v31
	v_cvt_pk_f32_fp8_sdwa v[102:103], v31 src0_sel:WORD_1
	v_pk_add_f32 v[72:73], v[72:73], v[96:97]
	v_pk_add_f32 v[74:75], v[74:75], v[98:99]
	v_pk_add_f32 v[78:79], v[78:79], v[100:101]
	v_pk_add_f32 v[82:83], v[82:83], v[102:103]
	v_cvt_pk_f32_fp8_e32 v[96:97], v32
	v_cvt_pk_f32_fp8_sdwa v[98:99], v32 src0_sel:WORD_1
	v_cvt_pk_f32_fp8_e32 v[100:101], v33
	v_cvt_pk_f32_fp8_sdwa v[102:103], v33 src0_sel:WORD_1
	v_pk_add_f32 v[64:65], v[64:65], v[96:97]
	v_pk_add_f32 v[66:67], v[66:67], v[98:99]
	v_pk_add_f32 v[68:69], v[68:69], v[100:101]
	v_pk_add_f32 v[70:71], v[70:71], v[102:103]
	s_waitcnt vmcnt(3)
	v_cvt_pk_f32_fp8_e32 v[96:97], v34
	v_cvt_pk_f32_fp8_sdwa v[98:99], v34 src0_sel:WORD_1
	v_cvt_pk_f32_fp8_e32 v[100:101], v35
	v_cvt_pk_f32_fp8_sdwa v[102:103], v35 src0_sel:WORD_1
	v_pk_add_f32 v[88:89], v[88:89], v[96:97]
	v_pk_add_f32 v[90:91], v[90:91], v[98:99]
	v_pk_add_f32 v[92:93], v[92:93], v[100:101]
	v_pk_add_f32 v[94:95], v[94:95], v[102:103]
	v_cvt_pk_f32_fp8_e32 v[96:97], v36
	v_cvt_pk_f32_fp8_sdwa v[98:99], v36 src0_sel:WORD_1
	v_cvt_pk_f32_fp8_e32 v[100:101], v37
	v_cvt_pk_f32_fp8_sdwa v[102:103], v37 src0_sel:WORD_1
	v_pk_add_f32 v[76:77], v[76:77], v[96:97]
	v_pk_add_f32 v[80:81], v[80:81], v[98:99]
	v_pk_add_f32 v[84:85], v[84:85], v[100:101]
	v_pk_add_f32 v[86:87], v[86:87], v[102:103]
	v_cvt_pk_f32_fp8_e32 v[96:97], v38
	v_cvt_pk_f32_fp8_sdwa v[98:99], v38 src0_sel:WORD_1
	v_cvt_pk_f32_fp8_e32 v[100:101], v39
	v_cvt_pk_f32_fp8_sdwa v[102:103], v39 src0_sel:WORD_1
	v_pk_add_f32 v[72:73], v[72:73], v[96:97]
	v_pk_add_f32 v[74:75], v[74:75], v[98:99]
	v_pk_add_f32 v[78:79], v[78:79], v[100:101]
	v_pk_add_f32 v[82:83], v[82:83], v[102:103]
	v_cvt_pk_f32_fp8_e32 v[96:97], v40
	v_cvt_pk_f32_fp8_sdwa v[98:99], v40 src0_sel:WORD_1
	v_cvt_pk_f32_fp8_e32 v[100:101], v41
	v_cvt_pk_f32_fp8_sdwa v[102:103], v41 src0_sel:WORD_1
	v_pk_add_f32 v[64:65], v[64:65], v[96:97]
	v_pk_add_f32 v[66:67], v[66:67], v[98:99]
	v_pk_add_f32 v[68:69], v[68:69], v[100:101]
	v_pk_add_f32 v[70:71], v[70:71], v[102:103]
	s_waitcnt vmcnt(1)
	v_cvt_pk_f32_fp8_e32 v[96:97], v42
	v_cvt_pk_f32_fp8_sdwa v[98:99], v42 src0_sel:WORD_1
	v_cvt_pk_f32_fp8_e32 v[100:101], v43
	v_cvt_pk_f32_fp8_sdwa v[102:103], v43 src0_sel:WORD_1
	v_pk_add_f32 v[88:89], v[88:89], v[96:97]
	v_pk_add_f32 v[90:91], v[90:91], v[98:99]
	v_pk_add_f32 v[92:93], v[92:93], v[100:101]
	v_pk_add_f32 v[94:95], v[94:95], v[102:103]
	v_cvt_pk_f32_fp8_e32 v[96:97], v44
	v_cvt_pk_f32_fp8_sdwa v[98:99], v44 src0_sel:WORD_1
	v_cvt_pk_f32_fp8_e32 v[100:101], v45
	v_cvt_pk_f32_fp8_sdwa v[102:103], v45 src0_sel:WORD_1
	v_pk_add_f32 v[76:77], v[76:77], v[96:97]
	v_pk_add_f32 v[80:81], v[80:81], v[98:99]
	v_pk_add_f32 v[84:85], v[84:85], v[100:101]
	v_pk_add_f32 v[86:87], v[86:87], v[102:103]
	v_cvt_pk_f32_fp8_e32 v[96:97], v46
	v_cvt_pk_f32_fp8_sdwa v[98:99], v46 src0_sel:WORD_1
	v_cvt_pk_f32_fp8_e32 v[100:101], v47
	v_cvt_pk_f32_fp8_sdwa v[102:103], v47 src0_sel:WORD_1
	v_pk_add_f32 v[72:73], v[72:73], v[96:97]
	v_pk_add_f32 v[74:75], v[74:75], v[98:99]
	v_pk_add_f32 v[78:79], v[78:79], v[100:101]
	v_pk_add_f32 v[82:83], v[82:83], v[102:103]
	v_cvt_pk_f32_fp8_e32 v[96:97], v48
	v_cvt_pk_f32_fp8_sdwa v[98:99], v48 src0_sel:WORD_1
	v_cvt_pk_f32_fp8_e32 v[100:101], v49
	v_cvt_pk_f32_fp8_sdwa v[102:103], v49 src0_sel:WORD_1
	v_pk_add_f32 v[64:65], v[64:65], v[96:97]
	v_pk_add_f32 v[66:67], v[66:67], v[98:99]
	v_pk_add_f32 v[68:69], v[68:69], v[100:101]
	v_pk_add_f32 v[70:71], v[70:71], v[102:103]
	s_waitcnt vmcnt(0)
